# v55 stack + layer-1 list rebalanced so idle-slot workgroups (in-proj layer 1) absorb more conversion items
# baseline (speedup 1.0000x reference)
; #define LAS __attribute__((address_space(3)))
; __device__ __forceinline__ int f8w_bar_item(int wi, int i) {
;     if (i < F8W_BARQ0) return F8W_HOST0 - F8W_BARQ0 * F8W_BARW + wi + F8W_BARW * i;
;     return (wi < 896) ? (F8W_BAR0 + wi + 896 * (i - F8W_BARQ0)) : (F8W_BAR0 + 896 * (F8W_BARQ - 3) + (wi - 896) + 896 * (i - F8W_BARQ0)); }
; __device__ __forceinline__ void xcd_barrier_host(const XcdBarrier& b, Frame& F, unsigned epoch) {
;     asm volatile("s_waitcnt vmcnt(0)" ::: "memory");
;     __syncthreads();
;     volatile LAS unsigned* st = b.st;
;     if (F.wave == 0) {
;       if (threadIdx.x == 0) {
;         unsigned* bar = b.bar;
;         __builtin_amdgcn_s_waitcnt(0);
;         unsigned nloc = b.st[0], nx = b.st[1];
;         if (nloc == 0u) { xcd_barrier_complete(bar, b.x, nloc, nx); b.st[0] = nloc; b.st[1] = nx; }
;         const unsigned old = xb_add(&bar[XB_XSUB(b.x)], 1u);
;         const unsigned gen = old / nloc;
;         if (old + 1u == (gen + 1u) * nloc) {
;             __builtin_amdgcn_fence(__ATOMIC_RELEASE, "agent");
;             asm volatile("s_waitcnt vmcnt(0)" ::: "memory");
;             const unsigned og = xb_add(&bar[XB_TOP], 1u);
;             const unsigned tg = og / nx;
;             if (og + 1u == (tg + 1u) * nx) xb_add(&bar[XB_TOPGEN], 1u);
;             else XB_SPIN(xb_ld(&bar[XB_TOPGEN]) == tg, bar);
;             __builtin_amdgcn_fence(__ATOMIC_ACQUIRE, "agent");
;             xb_add(&bar[XB_XGEN(b.x)], 1u);
;             asm volatile("s_waitcnt vmcnt(0)" ::: "memory");
;         } else {
;             XB_SPIN(xb_ld(&bar[XB_XGEN(b.x)]) == gen, bar);
;             __builtin_amdgcn_fence(__ATOMIC_ACQUIRE, "agent");
;             asm volatile("s_waitcnt vmcnt(0)" ::: "memory");
;         }
;         st[2] = epoch;
;       }
;     } else {
;         const int wv = F.wave, wi = (int)blockIdx.x * 7 + wv - 1;
;         for (;;) {
;             if (st[2] == epoch) break;
;             const int i = (int)st[8 + wv];
;             if (i >= f8w_bar_count(wi)) { __builtin_amdgcn_s_sleep(2); continue; }
;             f8w_convert_one(F, f8w_bar_item(wi, i));
;             if (F.lane == 0) st[8 + wv] = (unsigned)(i + 1);
;             asm volatile("s_waitcnt lgkmcnt(0)" ::: "memory");
;         }
;     }
;     __syncthreads();
; }
.LBB0_207:
	s_and_b64 vcc, exec, s[0:1]
	s_cbranch_vccz .LBB0_279
	s_waitcnt vmcnt(0)
	s_cmp_lg_u32 s89, 0
	s_barrier
	s_cbranch_scc0 .LBB0_231
	s_add_i32 s0, 0, 0x20168
	v_mov_b32_e32 v1, s0
	ds_read_b32 v1, v1
	s_waitcnt lgkmcnt(0)
	v_cmp_eq_u32_e32 vcc, 2, v1
	s_cbranch_vccnz .LBB0_230
	s_lshl_b32 s0, s89, 2
	s_add_i32 s8, s0, 0
	s_add_i32 s12, s89, s33
	s_add_i32 s8, s8, 0x20160
	s_cmpk_gt_i32 s12, 0x380
	s_cselect_b64 s[4:5], -1, 0
	s_and_b64 s[0:1], s[4:5], exec
	s_cselect_b32 s9, 25, 18
	s_add_i32 s10, s12, 0x9bff
	s_add_i32 s11, s12, 0x837f
	s_addk_i32 s12, 0x1aff
	s_add_u32 s13, s58, 0x41400000
	s_addc_u32 s14, s59, 0
	v_lshlrev_b32_e32 v1, 2, v186
	s_add_u32 s15, s58, 0x2b400000
	s_mov_b32 s3, 0
	v_and_b32_e32 v1, 60, v1
	v_and_b32_e32 v76, 48, v186
	s_addc_u32 s16, s59, 0
	v_cmp_eq_u32_e64 s[0:1], 0, v186
	v_mov_b32_e32 v77, s8
	s_add_i32 s17, 0, 0x200d8
	v_mov_b32_e32 v71, 0
	s_movk_i32 s18, 0xc8
	s_mov_b32 s19, 0xc3e00000
	s_add_i32 s20, 0, 0x20168
	v_mov_b32_e32 v78, 0x43e00000
	s_branch .LBB0_213

; #define LAS __attribute__((address_space(3)))
; __device__ __forceinline__ void f8w_bar_flush(Frame& F, volatile LAS unsigned* st, int upto) {
;     if (F.wave == 0) return;
;     const int wv = F.wave, wi = (int)blockIdx.x * 7 + wv - 1; int i = (int)st[8 + wv];
;     if (upto > F8W_BARQ0) upto = f8w_bar_count(wi);
;     if (i >= upto) return;
;     for (; i < upto; ++i) f8w_convert_one(F, f8w_bar_item(wi, i));
;     if (F.lane == 0) st[8 + wv] = (unsigned)upto;
; }
.LBB0_311:
	v_readlane_b32 s2, v254, 18
	v_readlane_b32 s3, v254, 19
	s_and_b64 s[2:3], s[2:3], s[6:7]
	s_cmp_gt_u32 s26, 63
	s_cselect_b64 s[4:5], -1, 0
	s_and_b64 s[2:3], s[2:3], s[4:5]
	v_and_b32_e32 v186, 63, v1
	s_andn2_b64 vcc, exec, s[2:3]
	s_cbranch_vccnz .LBB0_328
	s_lshl_b32 s2, s89, 2
	s_add_i32 s6, s2, 0
	s_add_i32 s6, s6, 0x20160
	v_mov_b32_e32 v2, s6
	ds_read_b32 v2, v2 offset:32
	v_readlane_b32 s2, v254, 14
	s_add_i32 s10, s89, s2
	s_cmpk_gt_i32 s10, 0x380
	s_cselect_b32 s7, 25, 18
	s_waitcnt lgkmcnt(0)
	v_cmp_le_i32_e32 vcc, s7, v2
	v_readfirstlane_b32 s8, v2
	s_cbranch_vccnz .LBB0_328
	s_cmpk_gt_i32 s10, 0x380
	s_cselect_b64 s[2:3], -1, 0
	s_add_i32 s9, s10, 0x9bff
	s_addk_i32 s10, 0x1aff
	s_add_u32 s11, s58, 0x41400000
	s_addc_u32 s12, s59, 0
	s_add_u32 s13, s58, 0x2b400000
	v_readlane_b32 s4, v254, 32
	v_lshlrev_b32_e32 v2, 2, v1
	v_and_b32_e32 v1, 48, v1
	s_addc_u32 s14, s59, 0
	s_add_i32 s4, s4, s89
	s_mul_i32 s5, s8, 0x380
	v_and_b32_e32 v72, 60, v2
	v_lshlrev_b32_e32 v73, 12, v1
	s_add_i32 s15, s4, s5
	s_branch .LBB0_315

; #define LAS __attribute__((address_space(3)))
; __device__ __forceinline__ unsigned xb_ld(unsigned* p)              { return __hip_atomic_load(p, __ATOMIC_RELAXED, __HIP_MEMORY_SCOPE_AGENT); }
; __device__ __forceinline__ unsigned xb_add(unsigned* p, unsigned v) { return __hip_atomic_fetch_add(p, v, __ATOMIC_RELAXED, __HIP_MEMORY_SCOPE_AGENT); }
; __device__ __forceinline__ void xcd_barrier_host(const XcdBarrier& b, Frame& F, unsigned epoch) {
;     asm volatile("s_waitcnt vmcnt(0)" ::: "memory");
;     __syncthreads();
;     volatile LAS unsigned* st = b.st;
;     if (F.wave == 0) {
;       if (threadIdx.x == 0) {
;         unsigned* bar = b.bar;
;         __builtin_amdgcn_s_waitcnt(0);
;         unsigned nloc = b.st[0], nx = b.st[1];
;         if (nloc == 0u) { xcd_barrier_complete(bar, b.x, nloc, nx); b.st[0] = nloc; b.st[1] = nx; }
;         const unsigned old = xb_add(&bar[XB_XSUB(b.x)], 1u);
;         const unsigned gen = old / nloc;
;         if (old + 1u == (gen + 1u) * nloc) {
;             __builtin_amdgcn_fence(__ATOMIC_RELEASE, "agent");
;             asm volatile("s_waitcnt vmcnt(0)" ::: "memory");
;             const unsigned og = xb_add(&bar[XB_TOP], 1u);
;             const unsigned tg = og / nx;
;             if (og + 1u == (tg + 1u) * nx) xb_add(&bar[XB_TOPGEN], 1u);
;             else XB_SPIN(xb_ld(&bar[XB_TOPGEN]) == tg, bar);
;             __builtin_amdgcn_fence(__ATOMIC_ACQUIRE, "agent");
;             xb_add(&bar[XB_XGEN(b.x)], 1u);
;             asm volatile("s_waitcnt vmcnt(0)" ::: "memory");
;         } else {
;             XB_SPIN(xb_ld(&bar[XB_XGEN(b.x)]) == gen, bar);
;             __builtin_amdgcn_fence(__ATOMIC_ACQUIRE, "agent");
;             asm volatile("s_waitcnt vmcnt(0)" ::: "memory");
;         }
;         st[2] = epoch;
;       }
;     } else {
;         const int wv = F.wave, wi = (int)blockIdx.x * 7 + wv - 1;
;         for (;;) {
;             if (st[2] == epoch) break;
;             const int i = (int)st[8 + wv];
;             if (i >= f8w_bar_count(wi)) { __builtin_amdgcn_s_sleep(2); continue; }
;             f8w_convert_one(F, f8w_bar_item(wi, i));
;             if (F.lane == 0) st[8 + wv] = (unsigned)(i + 1);
;             asm volatile("s_waitcnt lgkmcnt(0)" ::: "memory");
;         }
;     }
;     __syncthreads();
; }
.LBB0_376:
	s_and_b64 vcc, exec, s[0:1]
	s_cbranch_vccz .LBB0_448
	s_waitcnt vmcnt(0)
	s_cmp_lg_u32 s89, 0
	s_barrier
	s_cbranch_scc0 .LBB0_400
	v_mov_b32_e32 v1, s70
	ds_read_b32 v1, v1
	s_waitcnt lgkmcnt(0)
	v_cmp_eq_u32_e32 vcc, s38, v1
	s_cbranch_vccnz .LBB0_399
	v_readlane_b32 s0, v254, 14
	s_add_i32 s14, s89, s0
	s_lshl_b32 s0, s89, 2
	s_add_i32 s10, s0, 0
	s_add_i32 s10, s10, 0x20160
	s_cmpk_gt_i32 s14, 0x380
	s_cselect_b64 s[0:1], -1, 0
	s_and_b64 s[2:3], s[0:1], exec
	s_cselect_b32 s11, 25, 18
	s_add_i32 s12, s14, 0x9bff
	s_add_i32 s13, s14, 0x837f
	s_addk_i32 s14, 0x1aff
	s_add_u32 s2, s58, 0x41400000
	s_addc_u32 s3, s59, 0
	v_lshlrev_b32_e32 v1, 2, v186
	s_add_u32 s6, s58, 0x2b400000
	v_and_b32_e32 v1, 60, v1
	v_and_b32_e32 v72, -16, v186
	s_addc_u32 s7, s59, 0
	v_cmp_eq_u32_e64 s[4:5], 0, v186
	s_branch .LBB0_382

; __device__ __forceinline__ void hy_conv_item(Frame& F, int l, int c) {
;     ...
;     const bool host = (l == 0) && (F.G == 256) && (c == F.vcu);
;     const int hq0 = F8W_HOST0 + F.vcu * NWAVES + w; F8WItem hit; f32x4 hv[16]; int di = 0;
;     ...
;     hy_bf16x8 a00, a01, a10, a11, b0, b1, b2, b3;
;     HYC_LOAD(8 * w - 63, a00, a01, a10, a11, b0, b1, b2, b3);
;     for (int D = 8 * w - 63; D <= 8 * w + 7; ++D, ++di) {
;         if (host && (di & 15) == 0) {
;             if (di > 0) f8w_finish(hit, hv);
;             if (di < 16 * F8W_HOSTED) { hit = f8w_item(F, hq0 + (di >> 4) * (F.G * NWAVES)); f8w_load(hit, hv); } }
.LBB0_706:
	s_cmp_gt_u32 s15, 63
	s_cbranch_scc1 .LBB0_702
	s_mov_b32 s18, s20
	s_cmp_lg_u32 s100, 0
	s_cbranch_scc1 .Lhy_qok
	s_cmp_lt_u32 s20, 0x1180
	s_cselect_b32 s18, 0, 0x2300
	s_add_u32 s18, s18, 0xc280
	s_add_u32 s18, s18, s20

; #define LAS __attribute__((address_space(3)))
; __device__ __forceinline__ unsigned xb_ld(unsigned* p)              { return __hip_atomic_load(p, __ATOMIC_RELAXED, __HIP_MEMORY_SCOPE_AGENT); }
; __device__ __forceinline__ unsigned xb_add(unsigned* p, unsigned v) { return __hip_atomic_fetch_add(p, v, __ATOMIC_RELAXED, __HIP_MEMORY_SCOPE_AGENT); }
; __device__ __forceinline__ void xcd_barrier_host(const XcdBarrier& b, Frame& F, unsigned epoch) {
;     asm volatile("s_waitcnt vmcnt(0)" ::: "memory");
;     __syncthreads();
;     volatile LAS unsigned* st = b.st;
;     if (F.wave == 0) {
;       if (threadIdx.x == 0) {
;         unsigned* bar = b.bar;
;         __builtin_amdgcn_s_waitcnt(0);
;         unsigned nloc = b.st[0], nx = b.st[1];
;         if (nloc == 0u) { xcd_barrier_complete(bar, b.x, nloc, nx); b.st[0] = nloc; b.st[1] = nx; }
;         const unsigned old = xb_add(&bar[XB_XSUB(b.x)], 1u);
;         const unsigned gen = old / nloc;
;         if (old + 1u == (gen + 1u) * nloc) {
;             __builtin_amdgcn_fence(__ATOMIC_RELEASE, "agent");
;             asm volatile("s_waitcnt vmcnt(0)" ::: "memory");
;             const unsigned og = xb_add(&bar[XB_TOP], 1u);
;             const unsigned tg = og / nx;
;             if (og + 1u == (tg + 1u) * nx) xb_add(&bar[XB_TOPGEN], 1u);
;             else XB_SPIN(xb_ld(&bar[XB_TOPGEN]) == tg, bar);
;             __builtin_amdgcn_fence(__ATOMIC_ACQUIRE, "agent");
;             xb_add(&bar[XB_XGEN(b.x)], 1u);
;             asm volatile("s_waitcnt vmcnt(0)" ::: "memory");
;         } else {
;             XB_SPIN(xb_ld(&bar[XB_XGEN(b.x)]) == gen, bar);
;             __builtin_amdgcn_fence(__ATOMIC_ACQUIRE, "agent");
;             asm volatile("s_waitcnt vmcnt(0)" ::: "memory");
;         }
;         st[2] = epoch;
;       }
;     } else {
;         const int wv = F.wave, wi = (int)blockIdx.x * 7 + wv - 1;
;         for (;;) {
;             if (st[2] == epoch) break;
;             const int i = (int)st[8 + wv];
;             if (i >= f8w_bar_count(wi)) { __builtin_amdgcn_s_sleep(2); continue; }
;             f8w_convert_one(F, f8w_bar_item(wi, i));
;             if (F.lane == 0) st[8 + wv] = (unsigned)(i + 1);
;             asm volatile("s_waitcnt lgkmcnt(0)" ::: "memory");
;         }
;     }
;     __syncthreads();
; }
.LBB0_1311:
	s_and_b64 vcc, exec, s[0:1]
	s_cbranch_vccz .LBB0_1383
	s_waitcnt vmcnt(0)
	s_cmp_lg_u32 s89, 0
	s_barrier
	s_cbranch_scc0 .LBB0_1335
	v_mov_b32_e32 v1, s70
	ds_read_b32 v1, v1
	s_waitcnt lgkmcnt(0)
	v_cmp_eq_u32_e32 vcc, s38, v1
	s_cbranch_vccnz .LBB0_1334
	v_readlane_b32 s0, v254, 14
	s_add_i32 s14, s89, s0
	s_lshl_b32 s0, s89, 2
	s_add_i32 s10, s0, 0
	s_add_i32 s10, s10, 0x20160
	s_cmpk_gt_i32 s14, 0x380
	s_cselect_b64 s[0:1], -1, 0
	s_and_b64 s[2:3], s[0:1], exec
	s_cselect_b32 s11, 25, 18
	s_add_i32 s12, s14, 0x9bff
	s_add_i32 s13, s14, 0x837f
	s_addk_i32 s14, 0x1aff
	s_add_u32 s2, s80, 0x41400000
	s_addc_u32 s3, s81, 0
	v_lshlrev_b32_e32 v1, 2, v186
	s_add_u32 s6, s80, 0x2b400000
	v_and_b32_e32 v1, 60, v1
	v_and_b32_e32 v72, -16, v186
	s_addc_u32 s7, s81, 0
	v_cmp_eq_u32_e64 s[4:5], 0, v186
	s_branch .LBB0_1317

; #define LAS __attribute__((address_space(3)))
; __device__ __forceinline__ void f8w_bar_flush(Frame& F, volatile LAS unsigned* st, int upto) {
;     if (F.wave == 0) return;
;     const int wv = F.wave, wi = (int)blockIdx.x * 7 + wv - 1; int i = (int)st[8 + wv];
;     if (upto > F8W_BARQ0) upto = f8w_bar_count(wi);
;     if (i >= upto) return;
;     for (; i < upto; ++i) f8w_convert_one(F, f8w_bar_item(wi, i));
;     if (F.lane == 0) st[8 + wv] = (unsigned)upto;
; }
; __global__ void __launch_bounds__(NTHR, 2) fwd_kernel(Args args) {
;     ...
;         if (hostbar) { frame_fence(F); f8w_bar_flush(F, bar.st, l == 0 ? F8W_BARQ0 : F8W_BARQ0 + F8W_BARQ); }
.LBB0_1507:
	v_readlane_b32 s0, v254, 12
	v_readlane_b32 s1, v254, 13
	s_andn2_b64 vcc, exec, s[0:1]
	s_cbranch_vccnz .LBB0_1525
	v_readlane_b32 s0, v254, 8
	v_readlane_b32 s1, v254, 9
	v_mov_b32_e32 v2, v0
	v_writelane_b32 v254, s0, 8
	s_nop 1
	v_writelane_b32 v254, s1, 9
	s_movk_i32 s0, 0x100
	s_nop 0
	v_readfirstlane_b32 s0, v2
	s_ashr_i32 s89, s0, 6
	s_cmp_lt_u32 s0, 64
	v_and_b32_e32 v186, 63, v2
	s_cbranch_scc1 .LBB0_1525
	v_readlane_b32 s0, v254, 14
	s_add_i32 s8, s89, s0
	s_lshl_b32 s0, s89, 2
	s_add_i32 s4, s0, 0
	s_add_i32 s4, s4, 0x20160
	v_mov_b32_e32 v1, s4
	ds_read_b32 v1, v1 offset:32
	v_readlane_b32 s0, v254, 57
	s_cmpk_gt_i32 s8, 0x380
	v_readlane_b32 s1, v254, 58
	s_cselect_b32 s2, 25, 18
	s_and_b64 s[0:1], s[0:1], exec
	s_cselect_b32 s5, 15, s2
	s_waitcnt lgkmcnt(0)
	v_cmp_le_i32_e32 vcc, s5, v1
	v_readfirstlane_b32 s6, v1
	s_cbranch_vccnz .LBB0_1525
	s_cmpk_gt_i32 s8, 0x380
	s_cselect_b64 s[0:1], -1, 0
	s_add_i32 s7, s8, 0x9bff
	s_addk_i32 s8, 0x1aff
	s_add_u32 s9, s80, 0x41400000
	s_addc_u32 s10, s81, 0
	s_add_u32 s11, s80, 0x2b400000
	v_readlane_b32 s2, v254, 32
	v_lshlrev_b32_e32 v1, 2, v2
	v_and_b32_e32 v72, 48, v2
	s_addc_u32 s12, s81, 0
	s_add_i32 s2, s2, s89
	s_mul_i32 s3, s6, 0x380
	v_and_b32_e32 v1, 60, v1
	v_lshlrev_b32_e32 v73, 12, v72
	s_add_i32 s13, s2, s3
	s_branch .LBB0_1512

; #define LAS __attribute__((address_space(3)))
; __device__ __forceinline__ unsigned xb_ld(unsigned* p)              { return __hip_atomic_load(p, __ATOMIC_RELAXED, __HIP_MEMORY_SCOPE_AGENT); }
; __device__ __forceinline__ unsigned xb_add(unsigned* p, unsigned v) { return __hip_atomic_fetch_add(p, v, __ATOMIC_RELAXED, __HIP_MEMORY_SCOPE_AGENT); }
; __device__ __forceinline__ void xcd_barrier_host(const XcdBarrier& b, Frame& F, unsigned epoch) {
;     asm volatile("s_waitcnt vmcnt(0)" ::: "memory");
;     __syncthreads();
;     volatile LAS unsigned* st = b.st;
;     if (F.wave == 0) {
;       if (threadIdx.x == 0) {
;         unsigned* bar = b.bar;
;         __builtin_amdgcn_s_waitcnt(0);
;         unsigned nloc = b.st[0], nx = b.st[1];
;         if (nloc == 0u) { xcd_barrier_complete(bar, b.x, nloc, nx); b.st[0] = nloc; b.st[1] = nx; }
;         const unsigned old = xb_add(&bar[XB_XSUB(b.x)], 1u);
;         const unsigned gen = old / nloc;
;         if (old + 1u == (gen + 1u) * nloc) {
;             __builtin_amdgcn_fence(__ATOMIC_RELEASE, "agent");
;             asm volatile("s_waitcnt vmcnt(0)" ::: "memory");
;             const unsigned og = xb_add(&bar[XB_TOP], 1u);
;             const unsigned tg = og / nx;
;             if (og + 1u == (tg + 1u) * nx) xb_add(&bar[XB_TOPGEN], 1u);
;             else XB_SPIN(xb_ld(&bar[XB_TOPGEN]) == tg, bar);
;             __builtin_amdgcn_fence(__ATOMIC_ACQUIRE, "agent");
;             xb_add(&bar[XB_XGEN(b.x)], 1u);
;             asm volatile("s_waitcnt vmcnt(0)" ::: "memory");
;         } else {
;             XB_SPIN(xb_ld(&bar[XB_XGEN(b.x)]) == gen, bar);
;             __builtin_amdgcn_fence(__ATOMIC_ACQUIRE, "agent");
;             asm volatile("s_waitcnt vmcnt(0)" ::: "memory");
;         }
;         st[2] = epoch;
;       }
;     } else {
;         const int wv = F.wave, wi = (int)blockIdx.x * 7 + wv - 1;
;         for (;;) {
;             if (st[2] == epoch) break;
;             const int i = (int)st[8 + wv];
;             if (i >= f8w_bar_count(wi)) { __builtin_amdgcn_s_sleep(2); continue; }
;             f8w_convert_one(F, f8w_bar_item(wi, i));
;             if (F.lane == 0) st[8 + wv] = (unsigned)(i + 1);
;             asm volatile("s_waitcnt lgkmcnt(0)" ::: "memory");
;         }
;     }
;     __syncthreads();
; }
.LBB0_1572:
	s_and_b64 vcc, exec, s[0:1]
	s_cbranch_vccz .LBB0_1644
	s_waitcnt vmcnt(0)
	s_cmp_lg_u32 s89, 0
	s_waitcnt lgkmcnt(0)
	s_barrier
	s_cbranch_scc0 .LBB0_1596
	v_mov_b32_e32 v1, s70
	ds_read_b32 v1, v1
	s_waitcnt lgkmcnt(0)
	v_cmp_eq_u32_e32 vcc, s38, v1
	s_cbranch_vccnz .LBB0_1595
	v_readlane_b32 s0, v254, 14
	s_add_i32 s14, s89, s0
	s_lshl_b32 s0, s89, 2
	s_add_i32 s10, s0, 0
	s_add_i32 s10, s10, 0x20160
	s_cmpk_gt_i32 s14, 0x380
	s_cselect_b64 s[0:1], -1, 0
	s_and_b64 s[2:3], s[0:1], exec
	s_cselect_b32 s11, 25, 18
	s_add_i32 s12, s14, 0x9bff
	s_add_i32 s13, s14, 0x837f
	s_addk_i32 s14, 0x1aff
	s_add_u32 s2, s80, 0x41400000
	s_addc_u32 s3, s81, 0
	v_lshlrev_b32_e32 v1, 2, v186
	s_add_u32 s6, s80, 0x2b400000
	v_and_b32_e32 v1, 60, v1
	v_and_b32_e32 v72, -16, v186
	s_addc_u32 s7, s81, 0
	v_cmp_eq_u32_e64 s[4:5], 0, v186
	s_branch .LBB0_1578

; #define LAS __attribute__((address_space(3)))
; __device__ __forceinline__ unsigned xb_ld(unsigned* p)              { return __hip_atomic_load(p, __ATOMIC_RELAXED, __HIP_MEMORY_SCOPE_AGENT); }
; __device__ __forceinline__ unsigned xb_add(unsigned* p, unsigned v) { return __hip_atomic_fetch_add(p, v, __ATOMIC_RELAXED, __HIP_MEMORY_SCOPE_AGENT); }
; __device__ __forceinline__ void xcd_barrier_host(const XcdBarrier& b, Frame& F, unsigned epoch) {
;     asm volatile("s_waitcnt vmcnt(0)" ::: "memory");
;     __syncthreads();
;     volatile LAS unsigned* st = b.st;
;     if (F.wave == 0) {
;       if (threadIdx.x == 0) {
;         unsigned* bar = b.bar;
;         __builtin_amdgcn_s_waitcnt(0);
;         unsigned nloc = b.st[0], nx = b.st[1];
;         if (nloc == 0u) { xcd_barrier_complete(bar, b.x, nloc, nx); b.st[0] = nloc; b.st[1] = nx; }
;         const unsigned old = xb_add(&bar[XB_XSUB(b.x)], 1u);
;         const unsigned gen = old / nloc;
;         if (old + 1u == (gen + 1u) * nloc) {
;             __builtin_amdgcn_fence(__ATOMIC_RELEASE, "agent");
;             asm volatile("s_waitcnt vmcnt(0)" ::: "memory");
;             const unsigned og = xb_add(&bar[XB_TOP], 1u);
;             const unsigned tg = og / nx;
;             if (og + 1u == (tg + 1u) * nx) xb_add(&bar[XB_TOPGEN], 1u);
;             else XB_SPIN(xb_ld(&bar[XB_TOPGEN]) == tg, bar);
;             __builtin_amdgcn_fence(__ATOMIC_ACQUIRE, "agent");
;             xb_add(&bar[XB_XGEN(b.x)], 1u);
;             asm volatile("s_waitcnt vmcnt(0)" ::: "memory");
;         } else {
;             XB_SPIN(xb_ld(&bar[XB_XGEN(b.x)]) == gen, bar);
;             __builtin_amdgcn_fence(__ATOMIC_ACQUIRE, "agent");
;             asm volatile("s_waitcnt vmcnt(0)" ::: "memory");
;         }
;         st[2] = epoch;
;       }
;     } else {
;         const int wv = F.wave, wi = (int)blockIdx.x * 7 + wv - 1;
;         for (;;) {
;             if (st[2] == epoch) break;
;             const int i = (int)st[8 + wv];
;             if (i >= f8w_bar_count(wi)) { __builtin_amdgcn_s_sleep(2); continue; }
;             f8w_convert_one(F, f8w_bar_item(wi, i));
;             if (F.lane == 0) st[8 + wv] = (unsigned)(i + 1);
;             asm volatile("s_waitcnt lgkmcnt(0)" ::: "memory");
;         }
;     }
;     __syncthreads();
; }
.LBB0_2044:
	s_waitcnt vmcnt(0)
	s_cmp_lg_u32 s89, 0
	s_waitcnt lgkmcnt(0)
	s_barrier
	s_cbranch_scc0 .LBB0_2067
	v_mov_b32_e32 v1, s70
	ds_read_b32 v1, v1
	s_waitcnt lgkmcnt(0)
	v_cmp_eq_u32_e32 vcc, s36, v1
	s_cbranch_vccnz .LBB0_2066
	v_readlane_b32 s0, v254, 14
	s_add_i32 s14, s89, s0
	s_lshl_b32 s0, s89, 2
	s_add_i32 s10, s0, 0
	s_add_i32 s10, s10, 0x20160
	s_cmpk_gt_i32 s14, 0x380
	s_cselect_b64 s[0:1], -1, 0
	s_and_b64 s[2:3], s[0:1], exec
	s_cselect_b32 s11, 25, 18
	s_add_i32 s12, s14, 0x9bff
	s_add_i32 s13, s14, 0x837f
	s_addk_i32 s14, 0x1aff
	s_add_u32 s2, s58, 0x41400000
	s_addc_u32 s3, s59, 0
	v_lshlrev_b32_e32 v1, 2, v186
	s_add_u32 s6, s58, 0x2b400000
	v_and_b32_e32 v1, 60, v1
	v_and_b32_e32 v72, -16, v186
	s_addc_u32 s7, s59, 0
	v_cmp_eq_u32_e64 s[4:5], 0, v186
	s_branch .LBB0_2049
